# hdr
# baseline (speedup 1.0000x reference)
.LBB1_7:
	s_mov_b32 s19, s16
	s_cmp_lg_u32 s19, 0
	s_cbranch_scc1 .Lhdr_n0
	s_setprio 3
	s_branch .LBB1_12
.Lhdr_n0:
	s_cmp_lg_u32 s19, 1
	s_cbranch_scc1 .Lhdr_n1
	s_setprio 2
	s_branch .LBB1_12
.Lhdr_n1:
	s_cmp_lg_u32 s19, 2
	s_cbranch_scc1 .Lhdr_n2
	s_setprio 1
	s_branch .LBB1_12
.Lhdr_n2:
	s_setprio 0
.LBB1_12:
	s_and_b32 s12, s19, 1
	s_lshr_b32 s13, s19, 1
	s_add_i32 s16, s19, 1
	v_lshl_add_u32 v231, s13, 3, v221
	s_cmp_lg_u32 s19, 3
	s_cselect_b32 s17, s16, 3
	s_waitcnt lgkmcnt(2)
	v_lshlrev_b32_e32 v2, 7, v231
	s_lshl_b32 s14, s12, 6
	v_or3_b32 v160, v2, s14, v220
	s_waitcnt lgkmcnt(0)
	v_mov_b32_e32 v1, v220
	v_lshl_add_u64 v[2:3], v[160:161], 2, s[6:7]
	global_load_dword v232, v[2:3], off
	s_lshl_b32 s14, s17, 2
	s_and_b32 s14, s14, 24
	s_lshl_b32 s13, s13, 9
	v_lshrrev_b32_e32 v3, 5, v1
	s_cmp_eq_u32 s12, 0
	v_add_u32_e32 v2, s14, v221
	v_lshlrev_b32_e32 v206, 4, v3
	s_cselect_b64 s[14:15], -1, 0
	s_cmp_eq_u32 s12, 1
	v_add3_u32 v149, v228, s13, v206
	s_cselect_b64 s[12:13], -1, 0
	s_lshl_b32 s17, s17, 6
	s_and_b32 s17, s17, 64
	v_lshl_or_b32 v2, v2, 7, s17
	v_lshl_add_u32 v234, v1, 4, 0
	v_and_or_b32 v1, v1, 31, v2
	v_mul_lo_u32 v2, v1, 27
	v_add_u32_e32 v233, 0xc000, v234
	v_mad_u64_u32 v[204:205], s[20:21], v3, 14, v[2:3]
	v_add_u32_e32 v202, 13, v2
	s_waitcnt vmcnt(3)
	v_mul_f32_e32 v1, 0.15915494, v222
	v_cos_f32_e32 v2, v1
	v_sin_f32_e32 v1, v1
	v_add_f32_e32 v2, v2, v2
	v_cndmask_b32_e64 v3, v2, v1, s[0:1]
	v_mul_f32_e32 v1, v1, v2
	v_fma_f32 v2, v2, v2, -2.0
	v_cndmask_b32_e64 v4, v2, v1, s[0:1]
	v_mul_f32_e32 v207, v1, v2
	v_fma_f32 v208, v2, v2, -2.0
	v_mul_f32_e32 v2, 0.15915494, v182
	v_cvt_pk_fp8_f32 v131, v225, v3
	v_cos_f32_e32 v3, v2
	v_sin_f32_e32 v2, v2
	v_cndmask_b32_e64 v1, v208, v207, s[0:1]
	v_cvt_pk_fp8_f32 v131, v4, v1 op_sel:[0,0,1]
	v_add_f32_e32 v1, v3, v3
	v_cvt_pk_f16_f32 v1, v2, v1
	v_cvt_pk_fp8_f32 v128, v182, v183
	v_cvt_scalef32_pk_fp8_f16 v132, v1, 1.0
	v_pk_fma_f16 v1, v1, v1, -2.0 op_sel:[1,0,1] op_sel_hi:[1,1,0]
	v_mul_f32_e32 v0, 0.15915494, v183
	v_cvt_scalef32_pk_fp8_f16 v132, v1, 1.0 op_sel:[0,0,1]
	v_pk_fma_f16 v1, v1, v1, -2.0 op_sel:[0,1,1] op_sel_hi:[1,1,0]
	v_cos_f32_e32 v2, v0
	v_cvt_scalef32_pk_fp8_f16 v133, v1, 1.0
	v_pk_fma_f16 v1, v1, v1, -2.0 op_sel:[0,1,1] op_sel_hi:[1,1,0]
	v_sin_f32_e32 v0, v0
	v_cvt_scalef32_pk_fp8_f16 v133, v1, 1.0 op_sel:[0,0,1]
	v_pk_fma_f16 v1, v1, v1, -2.0 op_sel:[0,1,1] op_sel_hi:[1,1,0]
	s_nop 0
	v_cvt_scalef32_pk_fp8_f16 v134, v1, 1.0
	v_pk_fma_f16 v1, v1, v1, -2.0 op_sel:[0,1,1] op_sel_hi:[1,1,0]
	s_nop 0
	v_cvt_scalef32_pk_fp8_f16 v134, v1, 1.0 op_sel:[0,0,1]
	v_add_f32_e32 v1, v2, v2
	v_cvt_pk_f16_f32 v0, v0, v1
	v_cvt_scalef32_pk_fp8_f16 v135, v0, 1.0
	v_pk_fma_f16 v24, v0, v0, -2.0 op_sel:[1,0,1] op_sel_hi:[1,1,0]
	s_waitcnt vmcnt(2)
	v_mul_f32_e32 v0, 0.15915494, v224
	v_cos_f32_e32 v1, v0
	v_sin_f32_e32 v0, v0
	v_add_f32_e32 v1, v1, v1
	v_cndmask_b32_e64 v2, v1, v0, s[0:1]
	v_mul_f32_e32 v0, v0, v1
	v_fma_f32 v1, v1, v1, -2.0
	v_cndmask_b32_e64 v3, v1, v0, s[0:1]
	v_mul_f32_e32 v209, v0, v1
	v_fma_f32 v210, v1, v1, -2.0
	v_mul_f32_e32 v1, 0.15915494, v190
	s_waitcnt vmcnt(1)
	v_cvt_pk_fp8_f32 v19, v223, v2
	v_cos_f32_e32 v2, v1
	v_sin_f32_e32 v1, v1
	v_cndmask_b32_e64 v0, v210, v209, s[0:1]
	v_cvt_pk_fp8_f32 v19, v3, v0 op_sel:[0,0,1]
	v_add_f32_e32 v0, v2, v2
	v_cvt_pk_f16_f32 v0, v1, v0
	v_cvt_scalef32_pk_fp8_f16 v20, v0, 1.0
	v_pk_fma_f16 v0, v0, v0, -2.0 op_sel:[1,0,1] op_sel_hi:[1,1,0]
	v_mul_f32_e32 v1, 0.15915494, v191
	v_cvt_scalef32_pk_fp8_f16 v135, v24, 1.0 op_sel:[0,0,1]
	v_cvt_scalef32_pk_fp8_f16 v20, v0, 1.0 op_sel:[0,0,1]
	v_pk_fma_f16 v0, v0, v0, -2.0 op_sel:[0,1,1] op_sel_hi:[1,1,0]
	v_cos_f32_e32 v2, v1
	v_pk_fma_f16 v24, v24, v24, -2.0 op_sel:[0,1,1] op_sel_hi:[1,1,0]
	v_cvt_scalef32_pk_fp8_f16 v21, v0, 1.0
	v_pk_fma_f16 v0, v0, v0, -2.0 op_sel:[0,1,1] op_sel_hi:[1,1,0]
	v_sin_f32_e32 v1, v1
	v_pk_fma_f16 v35, v24, v24, -2.0 op_sel:[0,1,1] op_sel_hi:[1,1,0]
	v_cvt_pk_fp8_f32 v128, v184, v185 op_sel:[0,0,1]
	v_cvt_scalef32_pk_fp8_f16 v21, v0, 1.0 op_sel:[0,0,1]
	v_pk_fma_f16 v0, v0, v0, -2.0 op_sel:[0,1,1] op_sel_hi:[1,1,0]
	v_pk_fma_f16 v36, v35, v35, -2.0 op_sel:[0,1,1] op_sel_hi:[1,1,0]
	v_mul_f32_e32 v25, 0.15915494, v184
	v_cvt_pk_fp8_f32 v129, v198, v199
	v_cvt_pk_fp8_f32 v130, v178, v200
	v_cvt_pk_fp8_f32 v16, v190, v191
	v_cvt_pk_fp8_f32 v17, v194, v195
	v_cvt_pk_fp8_f32 v18, v186, v187
	v_cvt_scalef32_pk_fp8_f16 v22, v0, 1.0
	v_pk_fma_f16 v0, v0, v0, -2.0 op_sel:[0,1,1] op_sel_hi:[1,1,0]
	v_pk_fma_f16 v37, v36, v36, -2.0 op_sel:[0,1,1] op_sel_hi:[1,1,0]
	v_cvt_scalef32_pk_fp8_f16 v137, v36, 1.0
	v_cos_f32_e32 v36, v25
	v_cvt_scalef32_pk_fp8_f16 v22, v0, 1.0 op_sel:[0,0,1]
	v_add_f32_e32 v0, v2, v2
	v_sin_f32_e32 v25, v25
	v_cvt_pk_f16_f32 v0, v1, v0
	v_mov_b32_e32 v160, v204
	v_cvt_scalef32_pk_fp8_f16 v23, v0, 1.0
	v_pk_fma_f16 v34, v0, v0, -2.0 op_sel:[1,0,1] op_sel_hi:[1,1,0]
	ds_read_b128 v[26:29], v234
	ds_read_b128 v[30:33], v234 offset:1024
	ds_read_b128 v[8:11], v234 offset:2048
	ds_read_b128 v[12:15], v234 offset:3072
	ds_read_b128 v[0:3], v234 offset:4096
	ds_read_b128 v[4:7], v234 offset:5120
	ds_read_b128 v[152:155], v234 offset:6144
	ds_read_b128 v[156:159], v234 offset:7168
	ds_read_b128 v[96:99], v149
	ds_read_b128 v[100:103], v149 offset:32
	ds_read_b128 v[104:107], v149 offset:64
	ds_read_b128 v[108:111], v149 offset:96
	v_cvt_pk_fp8_f32 v129, v163, v201 op_sel:[0,0,1]
	v_cvt_pk_fp8_f32 v130, v179, v181 op_sel:[0,0,1]
	v_cvt_pk_fp8_f32 v16, v192, v193 op_sel:[0,0,1]
	v_cvt_pk_fp8_f32 v17, v196, v197 op_sel:[0,0,1]
	v_cvt_pk_fp8_f32 v18, v188, v189 op_sel:[0,0,1]
	v_cvt_scalef32_pk_fp8_f16 v136, v24, 1.0
	v_add_f32_e32 v24, v36, v36
	v_cvt_pk_f16_f32 v24, v25, v24
	v_pk_fma_f16 v25, v24, v24, -2.0 op_sel:[1,0,1] op_sel_hi:[1,1,0]
	v_cvt_scalef32_pk_fp8_f16 v138, v24, 1.0
	v_cvt_scalef32_pk_fp8_f16 v23, v34, 1.0 op_sel:[0,0,1]
	v_cvt_scalef32_pk_fp8_f16 v136, v35, 1.0 op_sel:[0,0,1]
	v_pk_fma_f16 v35, v25, v25, -2.0 op_sel:[0,1,1] op_sel_hi:[1,1,0]
	v_cvt_scalef32_pk_fp8_f16 v138, v25, 1.0 op_sel:[0,0,1]
	v_mul_f32_e32 v25, 0.15915494, v185
	s_waitcnt lgkmcnt(0)
	v_mfma_scale_f32_32x32x64_f8f6f4 v[112:127], v[26:33], v[16:23], v[96:111], v227, v226 op_sel_hi:[0,0,0]
	v_cvt_scalef32_pk_fp8_f16 v139, v35, 1.0
	v_pk_fma_f16 v35, v35, v35, -2.0 op_sel:[0,1,1] op_sel_hi:[1,1,0]
	s_nop 0
	v_pk_fma_f16 v24, v35, v35, -2.0 op_sel:[0,1,1] op_sel_hi:[1,1,0]
	ds_read_b128 v[64:67], v149 offset:128
	ds_read_b128 v[68:71], v149 offset:160
	ds_read_b128 v[72:75], v149 offset:192
	ds_read_b128 v[76:79], v149 offset:224
	v_cvt_scalef32_pk_fp8_f16 v140, v24, 1.0
	v_pk_fma_f16 v24, v24, v24, -2.0 op_sel:[0,1,1] op_sel_hi:[1,1,0]
	v_cvt_scalef32_pk_fp8_f16 v137, v37, 1.0 op_sel:[0,0,1]
	v_cvt_scalef32_pk_fp8_f16 v140, v24, 1.0 op_sel:[0,0,1]
	v_cvt_scalef32_pk_fp8_f16 v139, v35, 1.0 op_sel:[0,0,1]
	v_mfma_scale_f32_32x32x64_f8f6f4 v[96:111], v[26:33], v[128:135], v[96:111], v227, v226 op_sel_hi:[0,0,0]
	v_cos_f32_e32 v26, v25
	v_sin_f32_e32 v25, v25
	v_mul_f32_e32 v30, 0.15915494, v192
	v_mul_f32_e32 v31, 0.15915494, v193
	v_add_f32_e32 v24, v26, v26
	v_cvt_pk_f16_f32 v24, v25, v24
	v_cvt_scalef32_pk_fp8_f16 v141, v24, 1.0
	v_pk_fma_f16 v24, v24, v24, -2.0 op_sel:[1,0,1] op_sel_hi:[1,1,0]
	s_nop 0
	v_cvt_scalef32_pk_fp8_f16 v141, v24, 1.0 op_sel:[0,0,1]
	v_pk_fma_f16 v26, v24, v24, -2.0 op_sel:[0,1,1] op_sel_hi:[1,1,0]
	v_lshl_add_u64 v[24:25], v[160:161], 2, s[4:5]
	v_pk_fma_f16 v27, v26, v26, -2.0 op_sel:[0,1,1] op_sel_hi:[1,1,0]
	s_nop 0
	v_pk_fma_f16 v28, v27, v27, -2.0 op_sel:[0,1,1] op_sel_hi:[1,1,0]
	s_waitcnt lgkmcnt(0)
	v_mfma_scale_f32_32x32x64_f8f6f4 v[80:95], v[8:15], v[16:23], v[64:79], v227, v226 op_sel_hi:[0,0,0]
	global_load_dwordx4 v[182:185], v[24:25], off
	global_load_dwordx4 v[190:193], v[24:25], off offset:3456
	v_cos_f32_e32 v25, v31
	v_pk_fma_f16 v29, v28, v28, -2.0 op_sel:[0,1,1] op_sel_hi:[1,1,0]
	v_cvt_scalef32_pk_fp8_f16 v143, v28, 1.0
	v_cvt_scalef32_pk_fp8_f16 v142, v26, 1.0
	v_cvt_scalef32_pk_fp8_f16 v143, v29, 1.0 op_sel:[0,0,1]
	v_cvt_scalef32_pk_fp8_f16 v142, v27, 1.0 op_sel:[0,0,1]
	v_add_f32_e32 v150, v25, v25
	v_mfma_scale_f32_32x32x64_f8f6f4 v[64:79], v[8:15], v[128:135], v[64:79], v227, v226 op_sel_hi:[0,0,0]
	v_pk_fma_f16 v8, v34, v34, -2.0 op_sel:[0,1,1] op_sel_hi:[1,1,0]
	ds_read_b128 v[32:35], v149 offset:256
	ds_read_b128 v[36:39], v149 offset:288
	ds_read_b128 v[40:43], v149 offset:320
	ds_read_b128 v[44:47], v149 offset:352
	v_pk_fma_f16 v9, v8, v8, -2.0 op_sel:[0,1,1] op_sel_hi:[1,1,0]
	v_cvt_scalef32_pk_fp8_f16 v144, v8, 1.0
	v_pk_fma_f16 v10, v9, v9, -2.0 op_sel:[0,1,1] op_sel_hi:[1,1,0]
	v_cvt_scalef32_pk_fp8_f16 v144, v9, 1.0 op_sel:[0,0,1]
	v_pk_fma_f16 v11, v10, v10, -2.0 op_sel:[0,1,1] op_sel_hi:[1,1,0]
	v_cvt_scalef32_pk_fp8_f16 v145, v10, 1.0
	v_cos_f32_e32 v10, v30
	v_cvt_scalef32_pk_fp8_f16 v145, v11, 1.0 op_sel:[0,0,1]
	v_sin_f32_e32 v11, v30
	v_add_f32_e32 v8, v10, v10
	v_cvt_pk_f16_f32 v8, v11, v8
	v_pk_fma_f16 v9, v8, v8, -2.0 op_sel:[1,0,1] op_sel_hi:[1,1,0]
	v_cvt_scalef32_pk_fp8_f16 v146, v8, 1.0
	v_pk_fma_f16 v10, v9, v9, -2.0 op_sel:[0,1,1] op_sel_hi:[1,1,0]
	s_waitcnt lgkmcnt(0)
	v_mfma_scale_f32_32x32x64_f8f6f4 v[48:63], v[0:7], v[16:23], v[32:47], v227, v226 op_sel_hi:[0,0,0]
	v_cvt_scalef32_pk_fp8_f16 v147, v10, 1.0
	v_pk_fma_f16 v10, v10, v10, -2.0 op_sel:[0,1,1] op_sel_hi:[1,1,0]
	v_cvt_scalef32_pk_fp8_f16 v146, v9, 1.0 op_sel:[0,0,1]
	v_cvt_scalef32_pk_fp8_f16 v147, v10, 1.0 op_sel:[0,0,1]
	v_pk_fma_f16 v24, v10, v10, -2.0 op_sel:[0,1,1] op_sel_hi:[1,1,0]
	s_nop 0
	v_cvt_scalef32_pk_fp8_f16 v148, v24, 1.0
	v_pk_fma_f16 v24, v24, v24, -2.0 op_sel:[0,1,1] op_sel_hi:[1,1,0]
	s_nop 0
	v_cvt_scalef32_pk_fp8_f16 v148, v24, 1.0 op_sel:[0,0,1]
	v_mfma_scale_f32_32x32x64_f8f6f4 v[32:47], v[0:7], v[128:135], v[32:47], v227, v226 op_sel_hi:[0,0,0]
	ds_read_b128 v[0:3], v149 offset:384
	ds_read_b128 v[4:7], v149 offset:416
	ds_read_b128 v[8:11], v149 offset:448
	ds_read_b128 v[12:15], v149 offset:480
	v_sin_f32_e32 v149, v31
	s_nop 0
	v_cvt_pk_f16_f32 v150, v149, v150
	v_cvt_scalef32_pk_fp8_f16 v149, v150, 1.0
	v_pk_fma_f16 v150, v150, v150, -2.0 op_sel:[1,0,1] op_sel_hi:[1,1,0]
	s_nop 0
	v_pk_fma_f16 v160, v150, v150, -2.0 op_sel:[0,1,1] op_sel_hi:[1,1,0]
	v_cvt_scalef32_pk_fp8_f16 v149, v150, 1.0 op_sel:[0,0,1]
	v_pk_fma_f16 v164, v160, v160, -2.0 op_sel:[0,1,1] op_sel_hi:[1,1,0]
	s_nop 0
	v_pk_fma_f16 v150, v164, v164, -2.0 op_sel:[0,1,1] op_sel_hi:[1,1,0]
	s_waitcnt lgkmcnt(0)
	v_mfma_scale_f32_32x32x64_f8f6f4 v[16:31], v[152:159], v[16:23], v[0:15], v227, v226 op_sel_hi:[0,0,0]
	v_pk_fma_f16 v165, v150, v150, -2.0 op_sel:[0,1,1] op_sel_hi:[1,1,0]
	v_cvt_scalef32_pk_fp8_f16 v151, v150, 1.0
	v_cvt_scalef32_pk_fp8_f16 v150, v160, 1.0
	v_cvt_scalef32_pk_fp8_f16 v151, v165, 1.0 op_sel:[0,0,1]
	v_cvt_scalef32_pk_fp8_f16 v150, v164, 1.0 op_sel:[0,0,1]
	v_mfma_scale_f32_32x32x64_f8f6f4 v[0:15], v[152:159], v[128:135], v[0:15], v227, v226 op_sel_hi:[0,0,0]
	v_mul_f32_e32 v128, 0.15915494, v198
	v_cos_f32_e32 v129, v128
	v_sin_f32_e32 v128, v128
	v_mul_f32_e32 v133, 0.15915494, v199
	v_cos_f32_e32 v134, v133
	v_add_f32_e32 v129, v129, v129
	v_cvt_pk_f16_f32 v130, v128, v129
	v_pk_fma_f16 v131, v130, v130, -2.0 op_sel:[1,0,1] op_sel_hi:[1,1,0]
	v_sin_f32_e32 v133, v133
	v_pk_fma_f16 v128, v131, v131, -2.0 op_sel:[0,1,1] op_sel_hi:[1,1,0]
	s_nop 0
	v_pk_fma_f16 v132, v128, v128, -2.0 op_sel:[0,1,1] op_sel_hi:[1,1,0]
	v_cvt_scalef32_pk_fp8_f16 v129, v128, 1.0
	v_cvt_scalef32_pk_fp8_f16 v128, v130, 1.0
	v_add_f32_e32 v130, v134, v134
	v_cvt_scalef32_pk_fp8_f16 v128, v131, 1.0 op_sel:[0,0,1]
	v_cvt_pk_f16_f32 v130, v133, v130
	v_cvt_scalef32_pk_fp8_f16 v129, v132, 1.0 op_sel:[0,0,1]
	v_cvt_scalef32_pk_fp8_f16 v131, v130, 1.0
	v_pk_fma_f16 v133, v130, v130, -2.0 op_sel:[1,0,1] op_sel_hi:[1,1,0]
	v_pk_fma_f16 v132, v132, v132, -2.0 op_sel:[0,1,1] op_sel_hi:[1,1,0]
	ds_read_b128 v[152:155], v234 offset:8192
	ds_read_b128 v[156:159], v234 offset:9216
	ds_read_b128 v[164:167], v234 offset:10240
	ds_read_b128 v[168:171], v234 offset:11264
	ds_read_b128 v[236:239], v234 offset:12288
	ds_read_b128 v[240:243], v234 offset:13312
	v_cvt_scalef32_pk_fp8_f16 v130, v132, 1.0
	v_pk_fma_f16 v132, v132, v132, -2.0 op_sel:[0,1,1] op_sel_hi:[1,1,0]
	v_mul_f32_e32 v135, 0.15915494, v163
	s_waitcnt lgkmcnt(4)
	v_mfma_scale_f32_32x32x64_f8f6f4 v[96:111], v[152:159], v[136:143], v[96:111], v227, v226 op_sel_hi:[0,0,0]
	v_cvt_scalef32_pk_fp8_f16 v131, v133, 1.0 op_sel:[0,0,1]
	v_pk_fma_f16 v133, v133, v133, -2.0 op_sel:[0,1,1] op_sel_hi:[1,1,0]
	v_cvt_scalef32_pk_fp8_f16 v130, v132, 1.0 op_sel:[0,0,1]
	v_cvt_scalef32_pk_fp8_f16 v132, v133, 1.0
	v_pk_fma_f16 v133, v133, v133, -2.0 op_sel:[0,1,1] op_sel_hi:[1,1,0]
	ds_read_b128 v[244:247], v234 offset:14336
	ds_read_b128 v[248:251], v234 offset:15360
	v_pk_fma_f16 v134, v133, v133, -2.0 op_sel:[0,1,1] op_sel_hi:[1,1,0]
	v_cvt_scalef32_pk_fp8_f16 v132, v133, 1.0 op_sel:[0,0,1]
	v_cvt_scalef32_pk_fp8_f16 v133, v134, 1.0
	v_pk_fma_f16 v134, v134, v134, -2.0 op_sel:[0,1,1] op_sel_hi:[1,1,0]
	s_nop 0
	v_cvt_scalef32_pk_fp8_f16 v133, v134, 1.0 op_sel:[0,0,1]
	v_mfma_scale_f32_32x32x64_f8f6f4 v[112:127], v[152:159], v[144:151], v[112:127], v227, v226 op_sel_hi:[0,0,0]
	v_cos_f32_e32 v152, v135
	v_sin_f32_e32 v135, v135
	v_mul_f32_e32 v154, 0.15915494, v194
	v_cos_f32_e32 v155, v154
	v_add_f32_e32 v134, v152, v152
	v_cvt_pk_f16_f32 v152, v135, v134
	v_pk_fma_f16 v153, v152, v152, -2.0 op_sel:[1,0,1] op_sel_hi:[1,1,0]
	v_sin_f32_e32 v154, v154
	v_pk_fma_f16 v134, v153, v153, -2.0 op_sel:[0,1,1] op_sel_hi:[1,1,0]
	s_nop 0
	v_pk_fma_f16 v160, v134, v134, -2.0 op_sel:[0,1,1] op_sel_hi:[1,1,0]
	v_cvt_scalef32_pk_fp8_f16 v135, v134, 1.0
	v_cvt_scalef32_pk_fp8_f16 v134, v152, 1.0
	v_add_f32_e32 v152, v155, v155
	s_waitcnt lgkmcnt(4)
	v_mfma_scale_f32_32x32x64_f8f6f4 v[64:79], v[164:171], v[136:143], v[64:79], v227, v226 op_sel_hi:[0,0,0]
	v_mul_f32_e32 v157, 0.15915494, v195
	v_cvt_pk_f16_f32 v154, v154, v152
	v_cos_f32_e32 v158, v157
	v_pk_fma_f16 v155, v154, v154, -2.0 op_sel:[1,0,1] op_sel_hi:[1,1,0]
	v_sin_f32_e32 v157, v157
	v_pk_fma_f16 v152, v155, v155, -2.0 op_sel:[0,1,1] op_sel_hi:[1,1,0]
	v_cvt_scalef32_pk_fp8_f16 v134, v153, 1.0 op_sel:[0,0,1]
	v_pk_fma_f16 v156, v152, v152, -2.0 op_sel:[0,1,1] op_sel_hi:[1,1,0]
	v_cvt_scalef32_pk_fp8_f16 v153, v152, 1.0
	v_cvt_scalef32_pk_fp8_f16 v152, v154, 1.0
	v_add_f32_e32 v154, v158, v158
	v_mul_f32_e32 v159, 0.15915494, v196
	v_cvt_scalef32_pk_fp8_f16 v152, v155, 1.0 op_sel:[0,0,1]
	v_mfma_scale_f32_32x32x64_f8f6f4 v[80:95], v[164:171], v[144:151], v[80:95], v227, v226 op_sel_hi:[0,0,0]
	v_cvt_pk_f16_f32 v154, v157, v154
	v_cvt_scalef32_pk_fp8_f16 v153, v156, 1.0 op_sel:[0,0,1]
	v_cvt_scalef32_pk_fp8_f16 v155, v154, 1.0
	v_pk_fma_f16 v156, v156, v156, -2.0 op_sel:[0,1,1] op_sel_hi:[1,1,0]
	v_pk_fma_f16 v157, v154, v154, -2.0 op_sel:[1,0,1] op_sel_hi:[1,1,0]
	v_cvt_scalef32_pk_fp8_f16 v154, v156, 1.0
	v_pk_fma_f16 v156, v156, v156, -2.0 op_sel:[0,1,1] op_sel_hi:[1,1,0]
	v_cvt_scalef32_pk_fp8_f16 v155, v157, 1.0 op_sel:[0,0,1]
	v_pk_fma_f16 v157, v157, v157, -2.0 op_sel:[0,1,1] op_sel_hi:[1,1,0]
	v_cvt_scalef32_pk_fp8_f16 v154, v156, 1.0 op_sel:[0,0,1]
	v_cvt_scalef32_pk_fp8_f16 v156, v157, 1.0
	v_pk_fma_f16 v157, v157, v157, -2.0 op_sel:[0,1,1] op_sel_hi:[1,1,0]
	s_waitcnt lgkmcnt(0)
	v_mfma_scale_f32_32x32x64_f8f6f4 v[0:15], v[244:251], v[136:143], v[0:15], v227, v226 op_sel_hi:[0,0,0]
	v_cvt_scalef32_pk_fp8_f16 v156, v157, 1.0 op_sel:[0,0,1]
	v_pk_fma_f16 v158, v157, v157, -2.0 op_sel:[0,1,1] op_sel_hi:[1,1,0]
	v_cvt_scalef32_pk_fp8_f16 v135, v160, 1.0 op_sel:[0,0,1]
	v_cvt_scalef32_pk_fp8_f16 v157, v158, 1.0
	v_mfma_scale_f32_32x32x64_f8f6f4 v[32:47], v[236:243], v[136:143], v[32:47], v227, v226 op_sel_hi:[0,0,0]
	v_cos_f32_e32 v136, v159
	v_sin_f32_e32 v137, v159
	v_pk_fma_f16 v138, v158, v158, -2.0 op_sel:[0,1,1] op_sel_hi:[1,1,0]
	v_add_f32_e32 v136, v136, v136
	v_cvt_pk_f16_f32 v136, v137, v136
	v_pk_fma_f16 v137, v136, v136, -2.0 op_sel:[1,0,1] op_sel_hi:[1,1,0]
	v_cvt_scalef32_pk_fp8_f16 v157, v138, 1.0 op_sel:[0,0,1]
	v_pk_fma_f16 v138, v137, v137, -2.0 op_sel:[0,1,1] op_sel_hi:[1,1,0]
	s_nop 0
	v_pk_fma_f16 v180, v138, v138, -2.0 op_sel:[0,1,1] op_sel_hi:[1,1,0]
	v_cvt_scalef32_pk_fp8_f16 v159, v138, 1.0
	v_cvt_scalef32_pk_fp8_f16 v158, v136, 1.0
	v_cvt_scalef32_pk_fp8_f16 v159, v180, 1.0 op_sel:[0,0,1]
	v_cvt_scalef32_pk_fp8_f16 v158, v137, 1.0 op_sel:[0,0,1]
	v_mfma_scale_f32_32x32x64_f8f6f4 v[48:63], v[236:243], v[144:151], v[48:63], v227, v226 op_sel_hi:[0,0,0]
	v_mfma_scale_f32_32x32x64_f8f6f4 v[16:31], v[244:251], v[144:151], v[16:31], v227, v226 op_sel_hi:[0,0,0]
	ds_read_b128 v[140:143], v234 offset:16384
	ds_read_b128 v[144:147], v234 offset:17408
	ds_read_b128 v[236:239], v234 offset:18432
	ds_read_b128 v[240:243], v234 offset:19456
	ds_read_b128 v[170:173], v234 offset:20480
	ds_read_b128 v[174:177], v234 offset:21504
	s_waitcnt lgkmcnt(4)
	v_mfma_scale_f32_32x32x64_f8f6f4 v[96:111], v[140:147], v[128:135], v[96:111], v227, v226 op_sel_hi:[0,0,0]
	v_pk_fma_f16 v139, v160, v160, -2.0 op_sel:[0,1,1] op_sel_hi:[1,1,0]
	v_mov_b32_e32 v160, v204
	ds_read_b128 v[162:165], v234 offset:22528
	ds_read_b128 v[166:169], v234 offset:23552
	v_mul_f32_e32 v136, 0.15915494, v201
	v_cos_f32_e32 v137, v136
	v_sin_f32_e32 v136, v136
	v_mul_f32_e32 v150, 0.15915494, v186
	v_cos_f32_e32 v151, v150
	v_add_f32_e32 v137, v137, v137
	v_cvt_pk_f16_f32 v136, v136, v137
	v_pk_fma_f16 v138, v136, v136, -2.0 op_sel:[1,0,1] op_sel_hi:[1,1,0]
	v_cvt_scalef32_pk_fp8_f16 v137, v136, 1.0
	v_mfma_scale_f32_32x32x64_f8f6f4 v[112:127], v[140:147], v[152:159], v[112:127], v227, v226 op_sel_hi:[0,0,0]
	v_mul_f32_e32 v140, 0.15915494, v178
	v_cos_f32_e32 v141, v140
	v_sin_f32_e32 v140, v140
	v_mul_f32_e32 v143, 0.15915494, v200
	v_cos_f32_e32 v144, v143
	v_add_f32_e32 v141, v141, v141
	v_cvt_pk_f16_f32 v141, v140, v141
	v_sin_f32_e32 v143, v143
	v_cvt_scalef32_pk_fp8_f16 v140, v141, 1.0
	v_pk_fma_f16 v141, v141, v141, -2.0 op_sel:[1,0,1] op_sel_hi:[1,1,0]
	v_mul_f32_e32 v146, 0.15915494, v197
	v_pk_fma_f16 v142, v141, v141, -2.0 op_sel:[0,1,1] op_sel_hi:[1,1,0]
	v_cvt_scalef32_pk_fp8_f16 v140, v141, 1.0 op_sel:[0,0,1]
	v_cvt_scalef32_pk_fp8_f16 v141, v142, 1.0
	v_pk_fma_f16 v145, v142, v142, -2.0 op_sel:[0,1,1] op_sel_hi:[1,1,0]
	v_add_f32_e32 v142, v144, v144
	v_cvt_pk_f16_f32 v144, v143, v142
	v_lshl_add_u64 v[142:143], v[160:161], 2, s[4:5]
	global_load_dwordx4 v[198:201], v[142:143], off offset:16
	global_load_dwordx4 v[194:197], v[142:143], off offset:3472
	v_cvt_scalef32_pk_fp8_f16 v141, v145, 1.0 op_sel:[0,0,1]
	v_pk_fma_f16 v160, v144, v144, -2.0 op_sel:[1,0,1] op_sel_hi:[1,1,0]
	v_cvt_scalef32_pk_fp8_f16 v143, v144, 1.0
	v_pk_fma_f16 v144, v145, v145, -2.0 op_sel:[0,1,1] op_sel_hi:[1,1,0]
	v_cos_f32_e32 v145, v146
	v_sin_f32_e32 v146, v146
	v_pk_fma_f16 v148, v138, v138, -2.0 op_sel:[0,1,1] op_sel_hi:[1,1,0]
	v_cvt_scalef32_pk_fp8_f16 v136, v139, 1.0
	v_pk_fma_f16 v139, v139, v139, -2.0 op_sel:[0,1,1] op_sel_hi:[1,1,0]
	v_pk_fma_f16 v149, v148, v148, -2.0 op_sel:[0,1,1] op_sel_hi:[1,1,0]
	v_cvt_scalef32_pk_fp8_f16 v142, v144, 1.0
	v_pk_fma_f16 v144, v144, v144, -2.0 op_sel:[0,1,1] op_sel_hi:[1,1,0]
	v_cvt_scalef32_pk_fp8_f16 v137, v138, 1.0 op_sel:[0,0,1]
	v_cvt_scalef32_pk_fp8_f16 v136, v139, 1.0 op_sel:[0,0,1]
	v_pk_fma_f16 v138, v149, v149, -2.0 op_sel:[0,1,1] op_sel_hi:[1,1,0]
	v_cvt_scalef32_pk_fp8_f16 v142, v144, 1.0 op_sel:[0,0,1]
	v_add_f32_e32 v144, v145, v145
	v_cvt_scalef32_pk_fp8_f16 v139, v138, 1.0
	v_pk_fma_f16 v138, v138, v138, -2.0 op_sel:[0,1,1] op_sel_hi:[1,1,0]
	s_waitcnt lgkmcnt(4)
	v_mfma_scale_f32_32x32x64_f8f6f4 v[64:79], v[236:243], v[128:135], v[64:79], v227, v226 op_sel_hi:[0,0,0]
	v_cvt_pk_f16_f32 v144, v146, v144
	v_cvt_scalef32_pk_fp8_f16 v139, v138, 1.0 op_sel:[0,0,1]
	v_pk_fma_f16 v146, v144, v144, -2.0 op_sel:[1,0,1] op_sel_hi:[1,1,0]
	v_cvt_scalef32_pk_fp8_f16 v138, v148, 1.0
	v_cvt_scalef32_pk_fp8_f16 v145, v144, 1.0
	v_pk_fma_f16 v147, v180, v180, -2.0 op_sel:[0,1,1] op_sel_hi:[1,1,0]
	v_pk_fma_f16 v148, v146, v146, -2.0 op_sel:[0,1,1] op_sel_hi:[1,1,0]
	v_cvt_scalef32_pk_fp8_f16 v138, v149, 1.0 op_sel:[0,0,1]
	v_cvt_scalef32_pk_fp8_f16 v144, v147, 1.0
	v_pk_fma_f16 v147, v147, v147, -2.0 op_sel:[0,1,1] op_sel_hi:[1,1,0]
	v_pk_fma_f16 v149, v148, v148, -2.0 op_sel:[0,1,1] op_sel_hi:[1,1,0]
	v_cvt_scalef32_pk_fp8_f16 v145, v146, 1.0 op_sel:[0,0,1]
	v_mfma_scale_f32_32x32x64_f8f6f4 v[80:95], v[236:243], v[152:159], v[80:95], v227, v226 op_sel_hi:[0,0,0]
	v_pk_fma_f16 v146, v149, v149, -2.0 op_sel:[0,1,1] op_sel_hi:[1,1,0]
	v_cvt_scalef32_pk_fp8_f16 v144, v147, 1.0 op_sel:[0,0,1]
	v_cvt_scalef32_pk_fp8_f16 v147, v146, 1.0
	v_pk_fma_f16 v146, v146, v146, -2.0 op_sel:[0,1,1] op_sel_hi:[1,1,0]
	v_sin_f32_e32 v150, v150
	v_cvt_scalef32_pk_fp8_f16 v147, v146, 1.0 op_sel:[0,0,1]
	v_cvt_scalef32_pk_fp8_f16 v146, v148, 1.0
	v_add_f32_e32 v148, v151, v151
	v_mul_f32_e32 v151, 0.15915494, v187
	v_cvt_scalef32_pk_fp8_f16 v146, v149, 1.0 op_sel:[0,0,1]
	v_cvt_pk_f16_f32 v149, v150, v148
	v_cvt_scalef32_pk_fp8_f16 v148, v149, 1.0
	s_waitcnt lgkmcnt(0)
	v_mfma_scale_f32_32x32x64_f8f6f4 v[0:15], v[162:169], v[128:135], v[0:15], v227, v226 op_sel_hi:[0,0,0]
	v_pk_fma_f16 v149, v149, v149, -2.0 op_sel:[1,0,1] op_sel_hi:[1,1,0]
	v_cvt_scalef32_pk_fp8_f16 v143, v160, 1.0 op_sel:[0,0,1]
	v_pk_fma_f16 v150, v149, v149, -2.0 op_sel:[0,1,1] op_sel_hi:[1,1,0]
	v_cvt_scalef32_pk_fp8_f16 v148, v149, 1.0 op_sel:[0,0,1]
	v_cvt_scalef32_pk_fp8_f16 v149, v150, 1.0
	v_mfma_scale_f32_32x32x64_f8f6f4 v[32:47], v[170:177], v[128:135], v[32:47], v227, v226 op_sel_hi:[0,0,0]
	v_cos_f32_e32 v128, v151
	v_sin_f32_e32 v129, v151
	v_pk_fma_f16 v130, v150, v150, -2.0 op_sel:[0,1,1] op_sel_hi:[1,1,0]
	v_add_f32_e32 v128, v128, v128
	v_cvt_pk_f16_f32 v128, v129, v128
	v_pk_fma_f16 v203, v128, v128, -2.0 op_sel:[1,0,1] op_sel_hi:[1,1,0]
	v_cvt_scalef32_pk_fp8_f16 v151, v128, 1.0
	v_pk_fma_f16 v128, v130, v130, -2.0 op_sel:[0,1,1] op_sel_hi:[1,1,0]
	s_nop 0
	v_cvt_scalef32_pk_fp8_f16 v150, v128, 1.0
	v_pk_fma_f16 v128, v128, v128, -2.0 op_sel:[0,1,1] op_sel_hi:[1,1,0]
	v_cvt_scalef32_pk_fp8_f16 v149, v130, 1.0 op_sel:[0,0,1]
	v_cvt_scalef32_pk_fp8_f16 v151, v203, 1.0 op_sel:[0,0,1]
	v_cvt_scalef32_pk_fp8_f16 v150, v128, 1.0 op_sel:[0,0,1]
	v_mfma_scale_f32_32x32x64_f8f6f4 v[48:63], v[170:177], v[152:159], v[48:63], v227, v226 op_sel_hi:[0,0,0]
	v_mfma_scale_f32_32x32x64_f8f6f4 v[16:31], v[162:169], v[152:159], v[16:31], v227, v226 op_sel_hi:[0,0,0]
	v_pk_fma_f16 v130, v160, v160, -2.0 op_sel:[0,1,1] op_sel_hi:[1,1,0]
	s_nop 0
	v_pk_fma_f16 v131, v130, v130, -2.0 op_sel:[0,1,1] op_sel_hi:[1,1,0]
	ds_read_b128 v[152:155], v234 offset:24576
	ds_read_b128 v[156:159], v234 offset:25600
	ds_read_b128 v[162:165], v234 offset:26624
	ds_read_b128 v[166:169], v234 offset:27648
	v_pk_fma_f16 v128, v131, v131, -2.0 op_sel:[0,1,1] op_sel_hi:[1,1,0]
	v_mov_b32_e32 v160, v204
	v_pk_fma_f16 v132, v128, v128, -2.0 op_sel:[0,1,1] op_sel_hi:[1,1,0]
	v_cvt_scalef32_pk_fp8_f16 v129, v128, 1.0
	v_cvt_scalef32_pk_fp8_f16 v129, v132, 1.0 op_sel:[0,0,1]
	v_mul_f32_e32 v132, 0.15915494, v179
	v_sin_f32_e32 v133, v132
	v_cos_f32_e32 v132, v132
	v_cvt_scalef32_pk_fp8_f16 v128, v130, 1.0
	v_cvt_scalef32_pk_fp8_f16 v128, v131, 1.0 op_sel:[0,0,1]
	v_add_f32_e32 v130, v132, v132
	v_cvt_pk_f16_f32 v132, v133, v130
	v_pk_fma_f16 v133, v132, v132, -2.0 op_sel:[1,0,1] op_sel_hi:[1,1,0]
	s_nop 0
	v_pk_fma_f16 v130, v133, v133, -2.0 op_sel:[0,1,1] op_sel_hi:[1,1,0]
	s_waitcnt lgkmcnt(2)
	v_mfma_scale_f32_32x32x64_f8f6f4 v[96:111], v[152:159], v[136:143], v[96:111], v227, v226 op_sel_hi:[0,0,0]
	v_cvt_scalef32_pk_fp8_f16 v131, v130, 1.0
	v_pk_fma_f16 v134, v130, v130, -2.0 op_sel:[0,1,1] op_sel_hi:[1,1,0]
	v_cvt_scalef32_pk_fp8_f16 v130, v132, 1.0
	v_cvt_scalef32_pk_fp8_f16 v131, v134, 1.0 op_sel:[0,0,1]
	v_cvt_scalef32_pk_fp8_f16 v130, v133, 1.0 op_sel:[0,0,1]
	v_pk_fma_f16 v133, v134, v134, -2.0 op_sel:[0,1,1] op_sel_hi:[1,1,0]
	v_mul_f32_e32 v134, 0.15915494, v181
	v_cos_f32_e32 v135, v134
	v_sin_f32_e32 v134, v134
	v_cvt_scalef32_pk_fp8_f16 v132, v133, 1.0
	v_pk_fma_f16 v133, v133, v133, -2.0 op_sel:[0,1,1] op_sel_hi:[1,1,0]
	ds_read_b128 v[170:173], v234 offset:28672
	ds_read_b128 v[174:177], v234 offset:29696
	ds_read_b128 v[236:239], v234 offset:30720
	ds_read_b128 v[240:243], v234 offset:31744
	v_cvt_scalef32_pk_fp8_f16 v132, v133, 1.0 op_sel:[0,0,1]
	v_add_f32_e32 v133, v135, v135
	v_mfma_scale_f32_32x32x64_f8f6f4 v[112:127], v[152:159], v[144:151], v[112:127], v227, v226 op_sel_hi:[0,0,0]
	v_cvt_pk_f16_f32 v152, v134, v133
	v_mul_f32_e32 v153, 0.15915494, v188
	v_lshl_add_u64 v[134:135], v[160:161], 2, s[4:5]
	v_mul_f32_e32 v154, 0.15915494, v189
	global_load_dwordx4 v[178:181], v[134:135], off offset:32
	global_load_dwordx4 v[186:189], v[134:135], off offset:3488
	v_pk_fma_f16 v134, v152, v152, -2.0 op_sel:[1,0,1] op_sel_hi:[1,1,0]
	v_cvt_scalef32_pk_fp8_f16 v133, v152, 1.0
	v_pk_fma_f16 v152, v134, v134, -2.0 op_sel:[0,1,1] op_sel_hi:[1,1,0]
	v_cvt_scalef32_pk_fp8_f16 v133, v134, 1.0 op_sel:[0,0,1]
	v_pk_fma_f16 v155, v152, v152, -2.0 op_sel:[0,1,1] op_sel_hi:[1,1,0]
	s_nop 0
	v_pk_fma_f16 v134, v155, v155, -2.0 op_sel:[0,1,1] op_sel_hi:[1,1,0]
	s_nop 0
	v_pk_fma_f16 v156, v134, v134, -2.0 op_sel:[0,1,1] op_sel_hi:[1,1,0]
	v_cvt_scalef32_pk_fp8_f16 v135, v134, 1.0
	v_cvt_scalef32_pk_fp8_f16 v134, v152, 1.0
	v_pk_fma_f16 v152, v203, v203, -2.0 op_sel:[0,1,1] op_sel_hi:[1,1,0]
	v_cvt_scalef32_pk_fp8_f16 v134, v155, 1.0 op_sel:[0,0,1]
	v_pk_fma_f16 v155, v152, v152, -2.0 op_sel:[0,1,1] op_sel_hi:[1,1,0]
	s_waitcnt lgkmcnt(4)
	v_mfma_scale_f32_32x32x64_f8f6f4 v[64:79], v[162:169], v[136:143], v[64:79], v227, v226 op_sel_hi:[0,0,0]
	v_cvt_scalef32_pk_fp8_f16 v135, v156, 1.0 op_sel:[0,0,1]
	v_pk_fma_f16 v156, v155, v155, -2.0 op_sel:[0,1,1] op_sel_hi:[1,1,0]
	s_nop 0
	v_pk_fma_f16 v157, v156, v156, -2.0 op_sel:[0,1,1] op_sel_hi:[1,1,0]
	v_mfma_scale_f32_32x32x64_f8f6f4 v[80:95], v[162:169], v[144:151], v[80:95], v227, v226 op_sel_hi:[0,0,0]
	v_cvt_scalef32_pk_fp8_f16 v165, v156, 1.0
	v_cos_f32_e32 v156, v153
	v_sin_f32_e32 v153, v153
	v_cvt_scalef32_pk_fp8_f16 v164, v152, 1.0
	v_add_f32_e32 v152, v156, v156
	v_cvt_pk_f16_f32 v152, v153, v152
	v_pk_fma_f16 v153, v152, v152, -2.0 op_sel:[1,0,1] op_sel_hi:[1,1,0]
	v_cvt_scalef32_pk_fp8_f16 v166, v152, 1.0
	v_cvt_scalef32_pk_fp8_f16 v164, v155, 1.0 op_sel:[0,0,1]
	v_pk_fma_f16 v155, v153, v153, -2.0 op_sel:[0,1,1] op_sel_hi:[1,1,0]
	v_cvt_scalef32_pk_fp8_f16 v166, v153, 1.0 op_sel:[0,0,1]
	s_waitcnt lgkmcnt(0)
	v_mfma_scale_f32_32x32x64_f8f6f4 v[0:15], v[236:243], v[136:143], v[0:15], v227, v226 op_sel_hi:[0,0,0]
	v_cos_f32_e32 v153, v154
	v_cvt_scalef32_pk_fp8_f16 v167, v155, 1.0
	v_pk_fma_f16 v155, v155, v155, -2.0 op_sel:[0,1,1] op_sel_hi:[1,1,0]
	v_sin_f32_e32 v154, v154
	v_pk_fma_f16 v152, v155, v155, -2.0 op_sel:[0,1,1] op_sel_hi:[1,1,0]
	s_nop 0
	v_cvt_scalef32_pk_fp8_f16 v168, v152, 1.0
	v_pk_fma_f16 v152, v152, v152, -2.0 op_sel:[0,1,1] op_sel_hi:[1,1,0]
	s_nop 0
	v_cvt_scalef32_pk_fp8_f16 v168, v152, 1.0 op_sel:[0,0,1]
	v_add_f32_e32 v152, v153, v153
	v_cvt_scalef32_pk_fp8_f16 v165, v157, 1.0 op_sel:[0,0,1]
	v_cvt_scalef32_pk_fp8_f16 v167, v155, 1.0 op_sel:[0,0,1]
	v_mfma_scale_f32_32x32x64_f8f6f4 v[32:47], v[170:177], v[136:143], v[32:47], v227, v226 op_sel_hi:[0,0,0]
	v_cvt_pk_f16_f32 v136, v154, v152
	v_cvt_scalef32_pk_fp8_f16 v169, v136, 1.0
	v_pk_fma_f16 v136, v136, v136, -2.0 op_sel:[1,0,1] op_sel_hi:[1,1,0]
	s_nop 0
	v_cvt_scalef32_pk_fp8_f16 v169, v136, 1.0 op_sel:[0,0,1]
	v_pk_fma_f16 v136, v136, v136, -2.0 op_sel:[0,1,1] op_sel_hi:[1,1,0]
	s_nop 0
	v_pk_fma_f16 v137, v136, v136, -2.0 op_sel:[0,1,1] op_sel_hi:[1,1,0]
	s_nop 0
	v_pk_fma_f16 v138, v137, v137, -2.0 op_sel:[0,1,1] op_sel_hi:[1,1,0]
	s_nop 0
	v_pk_fma_f16 v139, v138, v138, -2.0 op_sel:[0,1,1] op_sel_hi:[1,1,0]
	v_mfma_scale_f32_32x32x64_f8f6f4 v[48:63], v[170:177], v[144:151], v[48:63], v227, v226 op_sel_hi:[0,0,0]
	v_cvt_scalef32_pk_fp8_f16 v171, v138, 1.0
	v_cvt_scalef32_pk_fp8_f16 v170, v136, 1.0
	v_cvt_scalef32_pk_fp8_f16 v171, v139, 1.0 op_sel:[0,0,1]
	v_cvt_scalef32_pk_fp8_f16 v170, v137, 1.0 op_sel:[0,0,1]
	v_mfma_scale_f32_32x32x64_f8f6f4 v[16:31], v[236:243], v[144:151], v[16:31], v227, v226 op_sel_hi:[0,0,0]
	v_mul_f32_e32 v152, 0.15915494, v225
	ds_read_b128 v[136:139], v234 offset:32768
	ds_read_b128 v[140:143], v234 offset:33792
	v_cos_f32_e32 v153, v152
	v_sin_f32_e32 v152, v152
	v_mov_b32_e32 v205, v161
	s_waitcnt lgkmcnt(0)
	v_mfma_scale_f32_32x32x64_f8f6f4 v[96:111], v[136:143], v[128:135], v[96:111], v227, v226 op_sel_hi:[0,0,0]
	v_add_f32_e32 v153, v153, v153
	v_cvt_pk_f16_f32 v158, v152, v153
	v_mov_b32_e32 v203, v161
	v_cndmask_b32_e64 v162, 0, v222, s[0:1]
	v_mul_f32_e32 v163, 0.15915494, v223
	v_pk_fma_f16 v159, v158, v158, -2.0 op_sel:[1,0,1] op_sel_hi:[1,1,0]
	v_cndmask_b32_e64 v172, 0, v224, s[0:1]
	v_pk_fma_f16 v156, v159, v159, -2.0 op_sel:[0,1,1] op_sel_hi:[1,1,0]
	s_nop 0
	v_pk_fma_f16 v160, v156, v156, -2.0 op_sel:[0,1,1] op_sel_hi:[1,1,0]
	v_cvt_scalef32_pk_fp8_f16 v157, v156, 1.0
	v_cvt_scalef32_pk_fp8_f16 v156, v158, 1.0
	v_cvt_scalef32_pk_fp8_f16 v156, v159, 1.0 op_sel:[0,0,1]
	v_mfma_scale_f32_32x32x64_f8f6f4 v[112:127], v[136:143], v[164:171], v[112:127], v227, v226 op_sel_hi:[0,0,0]
	ds_read_b128 v[136:139], v234 offset:34816
	ds_read_b128 v[140:143], v234 offset:35840
	ds_read_b128 v[144:147], v234 offset:36864
	ds_read_b128 v[148:151], v234 offset:37888
	ds_read_b128 v[236:239], v234 offset:38912
	ds_read_b128 v[240:243], v234 offset:39936
	v_lshl_add_u64 v[152:153], v[204:205], 2, s[4:5]
	v_lshl_add_u64 v[154:155], v[202:203], 2, s[4:5]
	global_load_dword v225, v[152:153], off offset:48
	global_load_dword v222, v[154:155], off
	global_load_dword v224, v[154:155], off offset:3456
	global_load_dword v223, v[152:153], off offset:3504
	v_cvt_scalef32_pk_fp8_f16 v157, v160, 1.0 op_sel:[0,0,1]
	s_waitcnt lgkmcnt(4)
	v_mfma_scale_f32_32x32x64_f8f6f4 v[64:79], v[136:143], v[128:135], v[64:79], v227, v226 op_sel_hi:[0,0,0]
	v_mfma_scale_f32_32x32x64_f8f6f4 v[80:95], v[136:143], v[164:171], v[80:95], v227, v226 op_sel_hi:[0,0,0]
	v_mul_f32_e32 v136, v207, v208
	v_fma_f32 v137, v208, v208, -2.0
	v_cndmask_b32_e64 v138, v137, v136, s[0:1]
	v_mul_f32_e32 v136, v136, v137
	v_fma_f32 v137, v137, v137, -2.0
	v_cndmask_b32_e64 v139, v137, v136, s[0:1]
	v_cvt_pk_fp8_f32 v159, v138, v139
	v_mul_f32_e32 v136, v136, v137
	v_fma_f32 v137, v137, v137, -2.0
	v_cndmask_b32_e64 v136, v137, v136, s[0:1]
	v_cvt_pk_fp8_f32 v159, v136, v162 op_sel:[0,0,1]
	v_pk_fma_f16 v136, v160, v160, -2.0 op_sel:[0,1,1] op_sel_hi:[1,1,0]
	v_mov_b32_e32 v160, v161
	v_pk_fma_f16 v137, v136, v136, -2.0 op_sel:[0,1,1] op_sel_hi:[1,1,0]
	v_cvt_scalef32_pk_fp8_f16 v158, v136, 1.0
	v_cos_f32_e32 v136, v163
	v_cvt_scalef32_pk_fp8_f16 v158, v137, 1.0 op_sel:[0,0,1]
	v_sin_f32_e32 v137, v163
	s_waitcnt lgkmcnt(0)
	v_mfma_scale_f32_32x32x64_f8f6f4 v[0:15], v[236:243], v[128:135], v[0:15], v227, v226 op_sel_hi:[0,0,0]
	v_add_f32_e32 v136, v136, v136
	v_mov_b32_e32 v162, v161
	v_cvt_pk_f16_f32 v138, v137, v136
	v_pk_fma_f16 v139, v138, v138, -2.0 op_sel:[1,0,1] op_sel_hi:[1,1,0]
	s_nop 0
	v_pk_fma_f16 v136, v139, v139, -2.0 op_sel:[0,1,1] op_sel_hi:[1,1,0]
	v_mov_b32_e32 v163, v161
	v_pk_fma_f16 v140, v136, v136, -2.0 op_sel:[0,1,1] op_sel_hi:[1,1,0]
	v_cvt_scalef32_pk_fp8_f16 v137, v136, 1.0
	v_cvt_scalef32_pk_fp8_f16 v136, v138, 1.0
	v_cvt_scalef32_pk_fp8_f16 v136, v139, 1.0 op_sel:[0,0,1]
	v_mul_f32_e32 v138, v209, v210
	v_fma_f32 v139, v210, v210, -2.0
	v_cndmask_b32_e64 v141, v139, v138, s[0:1]
	v_mul_f32_e32 v138, v138, v139
	v_fma_f32 v142, v139, v139, -2.0
	v_cndmask_b32_e64 v143, v142, v138, s[0:1]
	v_cvt_pk_fp8_f32 v139, v141, v143
	v_mfma_scale_f32_32x32x64_f8f6f4 v[32:47], v[144:151], v[128:135], v[32:47], v227, v226 op_sel_hi:[0,0,0]
	v_mul_f32_e32 v128, v138, v142
	v_fma_f32 v129, v142, v142, -2.0
	v_cndmask_b32_e64 v128, v129, v128, s[0:1]
	v_cvt_pk_fp8_f32 v139, v128, v172 op_sel:[0,0,1]
	v_pk_fma_f16 v128, v140, v140, -2.0 op_sel:[0,1,1] op_sel_hi:[1,1,0]
	s_nop 0
	v_cvt_scalef32_pk_fp8_f16 v138, v128, 1.0
	v_pk_fma_f16 v128, v128, v128, -2.0 op_sel:[0,1,1] op_sel_hi:[1,1,0]
	v_cvt_scalef32_pk_fp8_f16 v137, v140, 1.0 op_sel:[0,0,1]
	v_cvt_scalef32_pk_fp8_f16 v138, v128, 1.0 op_sel:[0,0,1]
	v_mov_b32_e32 v140, v161
	v_mov_b32_e32 v141, v161
	v_mov_b32_e32 v142, v161
	v_mov_b32_e32 v143, v161
	v_mfma_scale_f32_32x32x64_f8f6f4 v[48:63], v[144:151], v[164:171], v[48:63], v227, v226 op_sel_hi:[0,0,0]
	v_mfma_scale_f32_32x32x64_f8f6f4 v[16:31], v[236:243], v[164:171], v[16:31], v227, v226 op_sel_hi:[0,0,0]
	ds_read_b128 v[128:131], v234 offset:40960
	ds_read_b128 v[132:135], v234 offset:41984
	s_waitcnt lgkmcnt(0)
	v_mfma_scale_f32_32x32x64_f8f6f4 v[96:111], v[128:135], v[156:163], v[96:111], v227, v226 op_sel_hi:[0,0,0]
	v_mfma_scale_f32_32x32x64_f8f6f4 v[112:127], v[128:135], v[136:143], v[112:127], v227, v226 op_sel_hi:[0,0,0]
	ds_read_b128 v[128:131], v234 offset:43008
	ds_read_b128 v[132:135], v234 offset:44032
	s_waitcnt lgkmcnt(0)
	v_mfma_scale_f32_32x32x64_f8f6f4 v[64:79], v[128:135], v[156:163], v[64:79], v227, v226 op_sel_hi:[0,0,0]
	v_mfma_scale_f32_32x32x64_f8f6f4 v[80:95], v[128:135], v[136:143], v[80:95], v227, v226 op_sel_hi:[0,0,0]
	ds_read_b128 v[128:131], v234 offset:45056
	ds_read_b128 v[132:135], v234 offset:46080
	s_waitcnt lgkmcnt(0)
	v_mfma_scale_f32_32x32x64_f8f6f4 v[32:47], v[128:135], v[156:163], v[32:47], v227, v226 op_sel_hi:[0,0,0]
	v_mfma_scale_f32_32x32x64_f8f6f4 v[48:63], v[128:135], v[136:143], v[48:63], v227, v226 op_sel_hi:[0,0,0]
	ds_read_b128 v[128:131], v234 offset:47104
	ds_read_b128 v[132:135], v234 offset:48128
	ds_read_b128 v[174:177], v234 offset:49152
	ds_read_b128 v[208:211], v234 offset:50176
	ds_read_b128 v[212:215], v234 offset:53248
	ds_read_b128 v[236:239], v234 offset:54272
	s_waitcnt lgkmcnt(4)
	v_mfma_scale_f32_32x32x64_f8f6f4 v[0:15], v[128:135], v[156:163], v[0:15], v227, v226 op_sel_hi:[0,0,0]
	v_mfma_scale_f32_32x32x64_f8f6f4 v[16:31], v[128:135], v[136:143], v[16:31], v227, v226 op_sel_hi:[0,0,0]
	v_cvt_pk_bf16_f32 v162, v96, v97 clamp
	v_cvt_pk_bf16_f32 v163, v98, v99 clamp
	v_cvt_pk_bf16_f32 v164, v100, v101 clamp
	v_cvt_pk_bf16_f32 v165, v102, v103 clamp
	v_cvt_pk_bf16_f32 v166, v112, v113 clamp
	v_cvt_pk_bf16_f32 v167, v114, v115 clamp
	v_cvt_pk_bf16_f32 v168, v116, v117 clamp
	v_cvt_pk_bf16_f32 v169, v118, v119 clamp
	v_cvt_pk_bf16_f32 v170, v104, v105 clamp
	v_cvt_pk_bf16_f32 v171, v106, v107 clamp
	v_cvt_pk_bf16_f32 v172, v108, v109 clamp
	v_add_u32_e32 v128, 0, v206
	v_cvt_pk_bf16_f32 v173, v110, v111 clamp
	v_add_u32_e32 v235, 0x18000, v128
	v_cvt_pk_bf16_f32 v202, v120, v121 clamp
	ds_read_b128 v[128:131], v235
	ds_read_b128 v[132:135], v235 offset:32
	ds_read_b128 v[136:139], v235 offset:64
	ds_read_b128 v[140:143], v235 offset:96
	v_cvt_pk_bf16_f32 v203, v122, v123 clamp
	ds_read_b128 v[96:99], v235 offset:128
	ds_read_b128 v[100:103], v235 offset:160
	ds_read_b128 v[104:107], v235 offset:192
	ds_read_b128 v[108:111], v235 offset:224
	v_cvt_pk_bf16_f32 v204, v124, v125 clamp
	v_cvt_pk_bf16_f32 v64, v64, v65
	s_waitcnt lgkmcnt(4)
	v_mfma_f32_32x32x16_bf16 v[144:159], v[174:177], v[166:169], v[128:143]
	v_cvt_pk_bf16_f32 v205, v126, v127 clamp
	ds_read_b128 v[240:243], v234 offset:57344
	ds_read_b128 v[244:247], v234 offset:58368
	ds_read_b128 v[248:251], v234 offset:61440
	ds_read_b128 v[252:255], v234 offset:62464
	v_cvt_pk_bf16_f32 v65, v74, v75 clamp
	v_cndmask_b32_e64 v230, v230, 0, s[14:15]
	v_mfma_f32_32x32x16_bf16 v[128:143], v[174:177], v[162:165], v[128:143]
	v_pk_max_i16 v174, v64, 0
	v_cvt_pk_bf16_f32 v175, v66, v67 clamp
	v_cvt_pk_bf16_f32 v176, v68, v69 clamp
	v_cvt_pk_bf16_f32 v177, v70, v71 clamp
	s_waitcnt lgkmcnt(4)
	v_mfma_f32_32x32x16_bf16 v[112:127], v[208:211], v[166:169], v[96:111]
	v_cvt_pk_bf16_f32 v80, v80, v81 clamp
	v_cvt_pk_bf16_f32 v81, v82, v83 clamp
	v_cvt_pk_bf16_f32 v82, v84, v85 clamp
	v_cvt_pk_bf16_f32 v83, v86, v87 clamp
	v_mfma_f32_32x32x16_bf16 v[96:111], v[208:211], v[162:165], v[96:111]
	v_cvt_pk_bf16_f32 v64, v72, v73 clamp
	v_cvt_pk_bf16_f32 v66, v76, v77 clamp
	v_cvt_pk_bf16_f32 v67, v78, v79 clamp
	v_cvt_pk_bf16_f32 v68, v88, v89 clamp
	v_cvt_pk_bf16_f32 v69, v90, v91 clamp
	v_cvt_pk_bf16_f32 v70, v92, v93 clamp
	v_cvt_pk_bf16_f32 v71, v94, v95 clamp
	v_add_u32_e32 v160, 0x14000, v234
	v_mfma_f32_32x32x16_bf16 v[128:143], v[212:215], v[170:173], v[128:143]
	v_mfma_f32_32x32x16_bf16 v[144:159], v[212:215], v[202:205], v[144:159]
	v_mfma_f32_32x32x16_bf16 v[96:111], v[236:239], v[170:173], v[96:111]
	v_mfma_f32_32x32x16_bf16 v[112:127], v[236:239], v[202:205], v[112:127]
	v_cvt_pk_bf16_f32 v76, v32, v33 clamp
	v_cvt_pk_bf16_f32 v77, v34, v35 clamp
	v_cvt_pk_bf16_f32 v78, v36, v37 clamp
	v_cvt_pk_bf16_f32 v79, v38, v39 clamp
	v_cvt_pk_bf16_f32 v88, v48, v49 clamp
	v_cvt_pk_bf16_f32 v89, v50, v51 clamp
	v_cvt_pk_bf16_f32 v90, v52, v53 clamp
	v_cvt_pk_bf16_f32 v91, v54, v55 clamp
	s_waitcnt lgkmcnt(3)
	v_mfma_f32_32x32x16_bf16 v[128:143], v[240:243], v[174:177], v[128:143]
	v_cvt_pk_bf16_f32 v72, v40, v41 clamp
	v_cvt_pk_bf16_f32 v73, v42, v43 clamp
	v_cvt_pk_bf16_f32 v74, v44, v45 clamp
	v_mfma_f32_32x32x16_bf16 v[144:159], v[240:243], v[80:83], v[144:159]
	ds_read_b128 v[92:95], v233 offset:16384
	ds_read_b128 v[208:211], v233 offset:17408
	ds_read_b128 v[236:239], v233 offset:20480
	ds_read_b128 v[240:243], v233 offset:21504
	v_cvt_pk_bf16_f32 v75, v46, v47 clamp
	v_cvt_pk_bf16_f32 v84, v56, v57 clamp
	v_cvt_pk_bf16_f32 v85, v58, v59 clamp
	s_waitcnt lgkmcnt(6)
	v_mfma_f32_32x32x16_bf16 v[96:111], v[244:247], v[174:177], v[96:111]
	v_cvt_pk_bf16_f32 v86, v60, v61 clamp
	v_cvt_pk_bf16_f32 v87, v62, v63 clamp
	v_mfma_f32_32x32x16_bf16 v[112:127], v[244:247], v[80:83], v[112:127]
	s_waitcnt lgkmcnt(5)
	v_mfma_f32_32x32x16_bf16 v[128:143], v[248:251], v[64:67], v[128:143]
	v_mfma_f32_32x32x16_bf16 v[144:159], v[248:251], v[68:71], v[144:159]
	s_waitcnt lgkmcnt(4)
	v_mfma_f32_32x32x16_bf16 v[96:111], v[252:255], v[64:67], v[96:111]
	v_mfma_f32_32x32x16_bf16 v[112:127], v[252:255], v[68:71], v[112:127]
	v_cvt_pk_bf16_f32 v206, v0, v1 clamp
	v_cvt_pk_bf16_f32 v207, v2, v3 clamp
	s_waitcnt lgkmcnt(2)
	v_mfma_f32_32x32x16_bf16 v[96:111], v[208:211], v[76:79], v[96:111]
	ds_read_b128 v[32:35], v233 offset:24576
	ds_read_b128 v[36:39], v233 offset:25600
	ds_read_b128 v[40:43], v233 offset:28672
	ds_read_b128 v[44:47], v233 offset:29696
	v_mfma_f32_32x32x16_bf16 v[112:127], v[208:211], v[88:91], v[112:127]
	v_cvt_pk_bf16_f32 v208, v4, v5 clamp
	v_cvt_pk_bf16_f32 v209, v6, v7 clamp
	v_cvt_pk_bf16_f32 v214, v16, v17 clamp
	v_cvt_pk_bf16_f32 v215, v18, v19 clamp
	v_cvt_pk_bf16_f32 v216, v20, v21 clamp
	v_cvt_pk_bf16_f32 v217, v22, v23 clamp
	v_mfma_f32_32x32x16_bf16 v[128:143], v[92:95], v[76:79], v[128:143]
	v_mfma_f32_32x32x16_bf16 v[144:159], v[92:95], v[88:91], v[144:159]
	v_cvt_pk_bf16_f32 v92, v8, v9 clamp
	v_cvt_pk_bf16_f32 v93, v10, v11 clamp
	v_cvt_pk_bf16_f32 v94, v12, v13 clamp
	v_cvt_pk_bf16_f32 v95, v14, v15 clamp
	v_cvt_pk_bf16_f32 v210, v24, v25 clamp
	v_cvt_pk_bf16_f32 v211, v26, v27 clamp
	v_cvt_pk_bf16_f32 v212, v28, v29 clamp
	v_cvt_pk_bf16_f32 v213, v30, v31 clamp
	s_waitcnt lgkmcnt(5)
	v_mfma_f32_32x32x16_bf16 v[128:143], v[236:239], v[72:75], v[128:143]
	v_mfma_f32_32x32x16_bf16 v[144:159], v[236:239], v[84:87], v[144:159]
	s_waitcnt lgkmcnt(4)
	v_mfma_f32_32x32x16_bf16 v[96:111], v[240:243], v[72:75], v[96:111]
	v_mfma_f32_32x32x16_bf16 v[112:127], v[240:243], v[84:87], v[112:127]
	s_waitcnt lgkmcnt(3)
	v_mfma_f32_32x32x16_bf16 v[128:143], v[32:35], v[206:209], v[128:143]
	ds_read_b128 v[0:3], v234 offset:51200
	ds_read_b128 v[236:239], v234 offset:52224
	ds_read_b128 v[240:243], v234 offset:55296
	ds_read_b128 v[244:247], v234 offset:56320
	v_mfma_f32_32x32x16_bf16 v[144:159], v[32:35], v[214:217], v[144:159]
	s_waitcnt lgkmcnt(6)
	v_mfma_f32_32x32x16_bf16 v[96:111], v[36:39], v[206:209], v[96:111]
	v_mfma_f32_32x32x16_bf16 v[112:127], v[36:39], v[214:217], v[112:127]
	s_waitcnt lgkmcnt(5)
	v_mfma_f32_32x32x16_bf16 v[128:143], v[40:43], v[92:95], v[128:143]
	v_mfma_f32_32x32x16_bf16 v[144:159], v[40:43], v[210:213], v[144:159]
	s_waitcnt lgkmcnt(4)
	v_mfma_f32_32x32x16_bf16 v[96:111], v[44:47], v[92:95], v[96:111]
	v_mfma_f32_32x32x16_bf16 v[112:127], v[44:47], v[210:213], v[112:127]
	ds_read_b128 v[32:35], v235 offset:256
	ds_read_b128 v[36:39], v235 offset:288
	ds_read_b128 v[40:43], v235 offset:320
	ds_read_b128 v[44:47], v235 offset:352
	s_nop 3
	v_cvt_pk_bf16_f32 v128, v128, v129 clamp
	v_cvt_pk_bf16_f32 v129, v130, v131 clamp
	v_cvt_pk_bf16_f32 v130, v132, v133 clamp
	v_cvt_pk_bf16_f32 v131, v134, v135 clamp
	s_waitcnt lgkmcnt(0)
	v_mfma_f32_32x32x16_bf16 v[48:63], v[0:3], v[166:169], v[32:47]
	v_cvt_pk_bf16_f32 v132, v144, v145 clamp
	v_cvt_pk_bf16_f32 v133, v146, v147 clamp
	v_cvt_pk_bf16_f32 v134, v148, v149 clamp
	v_cvt_pk_bf16_f32 v135, v150, v151 clamp
	v_mfma_f32_32x32x16_bf16 v[32:47], v[0:3], v[162:165], v[32:47]
	ds_read_b128 v[0:3], v235 offset:384
	ds_read_b128 v[4:7], v235 offset:416
	ds_read_b128 v[8:11], v235 offset:448
	ds_read_b128 v[12:15], v235 offset:480
	s_waitcnt lgkmcnt(0)
	v_mfma_f32_32x32x16_bf16 v[16:31], v[236:239], v[166:169], v[0:15]
	v_mfma_f32_32x32x16_bf16 v[0:15], v[236:239], v[162:165], v[0:15]
	ds_read_b128 v[162:165], v234 offset:59392
	ds_read_b128 v[166:169], v234 offset:60416
	ds_read_b128 v[236:239], v234 offset:63488
	ds_read_b128 v[248:251], v234 offset:64512
	v_mfma_f32_32x32x16_bf16 v[0:15], v[244:247], v[170:173], v[0:15]
	v_mfma_f32_32x32x16_bf16 v[32:47], v[240:243], v[170:173], v[32:47]
	v_mfma_f32_32x32x16_bf16 v[48:63], v[240:243], v[202:205], v[48:63]
	v_mfma_f32_32x32x16_bf16 v[16:31], v[244:247], v[202:205], v[16:31]
	s_waitcnt lgkmcnt(2)
	v_mfma_f32_32x32x16_bf16 v[0:15], v[166:169], v[174:177], v[0:15]
	v_cvt_pk_bf16_f32 v136, v136, v137 clamp
	v_cvt_pk_bf16_f32 v137, v138, v139 clamp
	v_cvt_pk_bf16_f32 v138, v140, v141 clamp
	v_cvt_pk_bf16_f32 v139, v142, v143 clamp
	v_cvt_pk_bf16_f32 v140, v152, v153 clamp
	v_mfma_f32_32x32x16_bf16 v[32:47], v[162:165], v[174:177], v[32:47]
	v_mfma_f32_32x32x16_bf16 v[48:63], v[162:165], v[80:83], v[48:63]
	v_mfma_f32_32x32x16_bf16 v[16:31], v[166:169], v[80:83], v[16:31]
	ds_read_b128 v[80:83], v233 offset:18432
	ds_read_b128 v[144:147], v233 offset:19456
	ds_read_b128 v[148:151], v233 offset:22528
	ds_read_b128 v[162:165], v233 offset:23552
	s_waitcnt lgkmcnt(4)
	v_mfma_f32_32x32x16_bf16 v[0:15], v[248:251], v[64:67], v[0:15]
	v_mfma_f32_32x32x16_bf16 v[32:47], v[236:239], v[64:67], v[32:47]
	v_cvt_pk_bf16_f32 v141, v154, v155 clamp
	v_cvt_pk_bf16_f32 v142, v156, v157 clamp
	v_cvt_pk_bf16_f32 v143, v158, v159 clamp
	v_mfma_f32_32x32x16_bf16 v[48:63], v[236:239], v[68:71], v[48:63]
	v_mfma_f32_32x32x16_bf16 v[16:31], v[248:251], v[68:71], v[16:31]
	s_waitcnt lgkmcnt(2)
	v_mfma_f32_32x32x16_bf16 v[0:15], v[144:147], v[76:79], v[0:15]
	v_mfma_f32_32x32x16_bf16 v[32:47], v[80:83], v[76:79], v[32:47]
	v_mfma_f32_32x32x16_bf16 v[48:63], v[80:83], v[88:91], v[48:63]
	ds_read_b128 v[64:67], v233 offset:26624
	ds_read_b128 v[68:71], v233 offset:27648
	ds_read_b128 v[76:79], v233 offset:30720
	ds_read_b128 v[80:83], v233 offset:31744
	v_mfma_f32_32x32x16_bf16 v[16:31], v[144:147], v[88:91], v[16:31]
	v_cvt_pk_bf16_f32 v96, v96, v97 clamp
	v_cvt_pk_bf16_f32 v97, v98, v99 clamp
	v_cvt_pk_bf16_f32 v98, v100, v101 clamp
	v_cvt_pk_bf16_f32 v99, v102, v103 clamp
	s_waitcnt lgkmcnt(4)
	v_mfma_f32_32x32x16_bf16 v[0:15], v[162:165], v[72:75], v[0:15]
	v_cvt_pk_bf16_f32 v100, v112, v113 clamp
	v_mfma_f32_32x32x16_bf16 v[32:47], v[148:151], v[72:75], v[32:47]
	v_cvt_pk_bf16_f32 v101, v114, v115 clamp
	v_cvt_pk_bf16_f32 v102, v116, v117 clamp
	v_cvt_pk_bf16_f32 v103, v118, v119 clamp
	v_mfma_f32_32x32x16_bf16 v[48:63], v[148:151], v[84:87], v[48:63]
	v_mfma_f32_32x32x16_bf16 v[16:31], v[162:165], v[84:87], v[16:31]
	s_waitcnt lgkmcnt(2)
	v_mfma_f32_32x32x16_bf16 v[0:15], v[68:71], v[206:209], v[0:15]
	ds_read_b128 v[84:87], v160
	ds_read_b128 v[112:115], v160 offset:1024
	ds_read_b128 v[116:119], v160 offset:2048
	ds_read_b128 v[144:147], v160 offset:3072
	v_mfma_f32_32x32x16_bf16 v[32:47], v[64:67], v[206:209], v[32:47]
	v_mfma_f32_32x32x16_bf16 v[48:63], v[64:67], v[214:217], v[48:63]
	v_cvt_pk_bf16_f32 v104, v104, v105 clamp
	v_cvt_pk_bf16_f32 v105, v106, v107 clamp
	v_cvt_pk_bf16_f32 v106, v108, v109 clamp
	v_cvt_pk_bf16_f32 v107, v110, v111 clamp
	v_mfma_f32_32x32x16_bf16 v[16:31], v[68:71], v[214:217], v[16:31]
	v_cvt_pk_bf16_f32 v108, v120, v121 clamp
	v_cvt_pk_bf16_f32 v109, v122, v123 clamp
	v_cvt_pk_bf16_f32 v110, v124, v125 clamp
	s_waitcnt lgkmcnt(4)
	v_mfma_f32_32x32x16_bf16 v[0:15], v[80:83], v[92:95], v[0:15]
	v_cvt_pk_bf16_f32 v111, v126, v127 clamp
	v_mfma_f32_32x32x16_bf16 v[32:47], v[76:79], v[92:95], v[32:47]
	v_mfma_f32_32x32x16_bf16 v[48:63], v[76:79], v[210:213], v[48:63]
	v_mfma_f32_32x32x16_bf16 v[16:31], v[80:83], v[210:213], v[16:31]
	s_waitcnt lgkmcnt(3)
	v_mfma_f32_4x4x4_16b_bf16 v[64:67], v[84:85], v[128:129], 0
	v_mfma_f32_4x4x4_16b_bf16 v[68:71], v[86:87], v[130:131], 0
	s_nop 7
	v_cvt_pk_bf16_f32 v32, v32, v33 clamp
	v_cvt_pk_bf16_f32 v33, v34, v35 clamp
	v_cvt_pk_bf16_f32 v34, v36, v37 clamp
	v_cvt_pk_bf16_f32 v35, v38, v39 clamp
	v_mfma_f32_4x4x4_16b_bf16 v[80:83], v[84:85], v[132:133], 0
	v_mfma_f32_4x4x4_16b_bf16 v[88:91], v[86:87], v[134:135], 0
	v_cvt_pk_bf16_f32 v48, v48, v49 clamp
	v_cvt_pk_bf16_f32 v49, v50, v51 clamp
	v_cvt_pk_bf16_f32 v50, v52, v53 clamp
	v_cvt_pk_bf16_f32 v51, v54, v55 clamp
	s_waitcnt lgkmcnt(2)
	v_mfma_f32_4x4x4_16b_bf16 v[64:67], v[112:113], v[136:137], v[64:67]
	v_mfma_f32_4x4x4_16b_bf16 v[68:71], v[114:115], v[138:139], v[68:71]
	v_cvt_pk_bf16_f32 v40, v40, v41 clamp
	v_cvt_pk_bf16_f32 v41, v42, v43 clamp
	v_cvt_pk_bf16_f32 v42, v44, v45 clamp
	v_cvt_pk_bf16_f32 v43, v46, v47 clamp
	v_mfma_f32_4x4x4_16b_bf16 v[80:83], v[112:113], v[140:141], v[80:83]
	v_mfma_f32_4x4x4_16b_bf16 v[88:91], v[114:115], v[142:143], v[88:91]
	s_waitcnt lgkmcnt(1)
	v_mfma_f32_4x4x4_16b_bf16 v[64:67], v[116:117], v[96:97], v[64:67]
	v_mfma_f32_4x4x4_16b_bf16 v[68:71], v[118:119], v[98:99], v[68:71]
	ds_read_b128 v[36:39], v160 offset:4096
	ds_read_b128 v[96:99], v160 offset:5120
	v_cvt_pk_bf16_f32 v0, v0, v1 clamp
	v_cvt_pk_bf16_f32 v1, v2, v3 clamp
	v_cvt_pk_bf16_f32 v2, v4, v5 clamp
	v_cvt_pk_bf16_f32 v3, v6, v7 clamp
	v_mfma_f32_4x4x4_16b_bf16 v[80:83], v[116:117], v[100:101], v[80:83]
	v_mfma_f32_4x4x4_16b_bf16 v[88:91], v[118:119], v[102:103], v[88:91]
	ds_read_b128 v[4:7], v160 offset:7168
	v_cvt_pk_bf16_f32 v12, v12, v13
	v_cvt_pk_bf16_f32 v24, v24, v25
	v_cvt_pk_bf16_f32 v25, v26, v27
	s_waitcnt lgkmcnt(3)
	v_mfma_f32_4x4x4_16b_bf16 v[64:67], v[144:145], v[104:105], v[64:67]
	v_mfma_f32_4x4x4_16b_bf16 v[68:71], v[146:147], v[106:107], v[68:71]
	v_cndmask_b32_e64 v219, v219, 0, s[14:15]
	v_cndmask_b32_e64 v218, v218, 0, s[14:15]
	v_mfma_f32_4x4x4_16b_bf16 v[80:83], v[144:145], v[108:109], v[80:83]
	v_mfma_f32_4x4x4_16b_bf16 v[88:91], v[146:147], v[110:111], v[88:91]
	s_waitcnt lgkmcnt(2)
	v_mfma_f32_4x4x4_16b_bf16 v[64:67], v[36:37], v[32:33], v[64:67]
	v_mfma_f32_4x4x4_16b_bf16 v[68:71], v[38:39], v[34:35], v[68:71]
	v_cvt_pk_bf16_f32 v34, v20, v21
	v_cvt_pk_bf16_f32 v35, v22, v23
	ds_read_b128 v[20:23], v160 offset:6144
	v_cvt_pk_bf16_f32 v32, v16, v17
	v_cvt_pk_bf16_f32 v33, v18, v19
	v_cvt_pk_bf16_f32 v16, v56, v57 clamp
	v_cvt_pk_bf16_f32 v17, v58, v59 clamp
	v_mfma_f32_4x4x4_16b_bf16 v[80:83], v[36:37], v[48:49], v[80:83]
	v_mfma_f32_4x4x4_16b_bf16 v[88:91], v[38:39], v[50:51], v[88:91]
	v_cvt_pk_bf16_f32 v18, v60, v61 clamp
	v_cvt_pk_bf16_f32 v19, v62, v63 clamp
	s_waitcnt lgkmcnt(2)
	v_mfma_f32_4x4x4_16b_bf16 v[64:67], v[96:97], v[40:41], v[64:67]
	v_mfma_f32_4x4x4_16b_bf16 v[68:71], v[98:99], v[42:43], v[68:71]
	v_mfma_f32_4x4x4_16b_bf16 v[80:83], v[96:97], v[16:17], v[80:83]
	v_mfma_f32_4x4x4_16b_bf16 v[88:91], v[98:99], v[18:19], v[88:91]
	v_cvt_pk_bf16_f32 v16, v8, v9
	v_cvt_pk_bf16_f32 v17, v10, v11
	v_pk_max_i16 v8, v24, 0
	v_pk_max_i16 v9, v25, 0
	v_cvt_pk_bf16_f32 v10, v28, v29 clamp
	v_cvt_pk_bf16_f32 v11, v30, v31 clamp
	s_waitcnt lgkmcnt(0)
	v_mfma_f32_4x4x4_16b_bf16 v[64:67], v[20:21], v[0:1], v[64:67]
	v_mfma_f32_4x4x4_16b_bf16 v[68:71], v[22:23], v[2:3], v[68:71]
	v_pk_max_i16 v0, v32, 0
	v_pk_max_i16 v1, v33, 0
	v_pk_max_i16 v2, v34, 0
	v_pk_max_i16 v3, v35, 0
	s_nop 1
	v_mfma_f32_4x4x4_16b_bf16 v[80:83], v[20:21], v[0:1], v[80:83]
	v_mfma_f32_4x4x4_16b_bf16 v[88:91], v[22:23], v[2:3], v[88:91]
	v_pk_max_i16 v0, v16, 0
	v_pk_max_i16 v1, v17, 0
	v_pk_max_i16 v2, v12, 0
	v_cvt_pk_bf16_f32 v3, v14, v15 clamp
	s_nop 1
	v_mfma_f32_4x4x4_16b_bf16 v[64:67], v[4:5], v[0:1], v[64:67]
	v_mfma_f32_4x4x4_16b_bf16 v[68:71], v[6:7], v[2:3], v[68:71]
	v_mfma_f32_4x4x4_16b_bf16 v[80:83], v[4:5], v[8:9], v[80:83]
	v_mfma_f32_4x4x4_16b_bf16 v[88:91], v[6:7], v[10:11], v[88:91]
	s_waitcnt vmcnt(10)
	s_nop 3
	v_pk_add_f32 v[64:65], v[64:65], v[68:69]
	v_pk_add_f32 v[80:81], v[80:81], v[88:89]
	v_add_f32_e32 v66, v66, v70
	v_add_f32_e32 v82, v82, v90
	s_nop 1
	v_permlane32_swap_b32_e32 v64, v80
	v_permlane32_swap_b32_e32 v65, v81
	v_permlane32_swap_b32_e32 v66, v82
	s_nop 0
	v_add_f32_e32 v64, v64, v80
	v_add_f32_e32 v65, v65, v81
	v_add_f32_e32 v66, v66, v82
	v_add_f32_e32 v3, s10, v64
	v_add_f32_e32 v4, s11, v65
	v_add_f32_e32 v5, s18, v66
	v_mul_f32_e32 v3, 0xbfb8aa3b, v3
	v_mul_f32_e32 v4, 0xbfb8aa3b, v4
	v_mul_f32_e32 v5, 0xbfb8aa3b, v5
	v_exp_f32_e32 v3, v3
	v_exp_f32_e32 v4, v4
	v_exp_f32_e32 v5, v5
	v_add_f32_e32 v3, 1.0, v3
	v_add_f32_e32 v4, 1.0, v4
	v_add_f32_e32 v5, 1.0, v5
	v_rcp_f32_e32 v3, v3
	v_rcp_f32_e32 v4, v4
	v_rcp_f32_e32 v5, v5
	v_fmac_f32_e32 v218, v232, v3
	v_fmac_f32_e32 v219, v232, v4
	v_fmac_f32_e32 v230, v232, v5
	s_andn2_b64 vcc, exec, s[12:13]
	s_cbranch_vccnz .LBB1_6
	v_add_f32_dpp v218, v218, v218 row_shr:1 row_mask:0xf bank_mask:0xf bound_ctrl:1
	v_add_f32_dpp v219, v219, v219 row_shr:1 row_mask:0xf bank_mask:0xf bound_ctrl:1
	v_add_f32_dpp v230, v230, v230 row_shr:1 row_mask:0xf bank_mask:0xf bound_ctrl:1
	v_add_f32_dpp v218, v218, v218 row_shr:2 row_mask:0xf bank_mask:0xf bound_ctrl:1
	v_add_f32_dpp v219, v219, v219 row_shr:2 row_mask:0xf bank_mask:0xf bound_ctrl:1
	v_add_f32_dpp v230, v230, v230 row_shr:2 row_mask:0xf bank_mask:0xf bound_ctrl:1
	v_add_f32_dpp v218, v218, v218 row_shr:4 row_mask:0xf bank_mask:0xf bound_ctrl:1
	v_add_f32_dpp v219, v219, v219 row_shr:4 row_mask:0xf bank_mask:0xf bound_ctrl:1
	v_add_f32_dpp v230, v230, v230 row_shr:4 row_mask:0xf bank_mask:0xf bound_ctrl:1
	v_add_f32_dpp v218, v218, v218 row_shr:8 row_mask:0xf bank_mask:0xf bound_ctrl:1
	v_add_f32_dpp v219, v219, v219 row_shr:8 row_mask:0xf bank_mask:0xf bound_ctrl:1
	v_add_f32_dpp v230, v230, v230 row_shr:8 row_mask:0xf bank_mask:0xf bound_ctrl:1
	v_mov_b32_e32 v0, 0
	v_mov_b32_e32 v1, 0
	v_mov_b32_e32 v5, 0
	v_mov_b32_dpp v0, v218 row_bcast:15 row_mask:0xa bank_mask:0xf
	v_mov_b32_dpp v1, v219 row_bcast:15 row_mask:0xa bank_mask:0xf
	v_mov_b32_dpp v5, v230 row_bcast:15 row_mask:0xa bank_mask:0xf
	v_lshl_add_u32 v6, v231, 1, v231
	v_ashrrev_i32_e32 v7, 31, v6
	v_add_f32_e32 v218, v218, v0
	v_add_f32_e32 v219, v219, v1
	v_add_f32_e32 v230, v230, v5
	v_mov_b32_e32 v0, 0
	v_mov_b32_e32 v1, 0
	v_mov_b32_e32 v5, 0
	v_mov_b32_dpp v0, v218 row_bcast:31 row_mask:0xc bank_mask:0xf
	v_mov_b32_dpp v1, v219 row_bcast:31 row_mask:0xc bank_mask:0xf
	v_mov_b32_dpp v5, v230 row_bcast:31 row_mask:0xc bank_mask:0xf
	v_lshl_add_u64 v[6:7], v[6:7], 2, s[8:9]
	v_cmp_eq_u32_e32 vcc, 63, v220
	v_add_f32_e32 v2, v218, v0
	v_add_f32_e32 v3, v219, v1
	v_add_f32_e32 v4, v230, v5
	s_and_saveexec_b64 s[12:13], vcc
	global_store_dwordx3 v[6:7], v[2:4], off
	s_branch .LBB1_5
.LBB1_17:
.LBB1_26:
	s_endpgm
